# MoE down projection: the units of the last partial round are split into two half-height units so the whole grid works in that round
# speedup vs baseline: 1.0016x; 1.0016x over previous
;     ...
;   moe_sched_build(p, sch, NTN, WHICH == 1);
;   const int total = sch->base[32];
;   const int slot = (bid & 7) * (nb >> 3) + (bid >> 3);
;   int ehint = 0;
;   auto decode = [&](int u, int& ee, int& m0, int& tn, int& cn) {
;     int e = ehint;
;     while (u >= sch->base[e + 1]) ++e;
;     ehint = e;
;     const int loc = u - sch->base[e];
;     const int mt = sch->mt[e];
;     ee = __builtin_amdgcn_readfirstlane(WHICH == 1 ? 31 - e : e); tn = __builtin_amdgcn_readfirstlane(loc / mt); m0 = __builtin_amdgcn_readfirstlane(loc % mt) * 256;
;     cn = __builtin_amdgcn_readfirstlane(sch->cnt[e]);
;   };
;     ...
;   typedef typename std::conditional<WHICH == 1, CfgMoe1F8T<(PMODE == 3 ? 1 : (PMODE == 4 ? 2 : 0))>, CfgMoe2F8>::type CfgT;
;   int u = slot;
;   if (u < total) {
;     int ee, m0, tn, cn; decode(u, ee, m0, tn, cn);
;     CfgT cur{p, ee, m0, tn, cn};
.LBB0_1589:
	s_or_b64 exec, exec, s[0:1]
	s_add_i32 s0, 0, 0x22090
	v_mov_b32_e32 v0, s0
	s_waitcnt lgkmcnt(0)
	s_barrier
	ds_read_b32 v0, v0
	s_waitcnt lgkmcnt(0)
	v_readfirstlane_b32 s28, v0
	s_mov_b32 s98, 0x7fffffff
	s_cmp_lg_u32 s96, 0x100
	s_cbranch_scc1 .Lts2_setup
	s_and_b32 s99, s28, 0xff
	s_add_i32 s100, s99, -1
	s_cmp_lt_u32 s100, 0x80
	s_cbranch_scc0 .Lts2_setup
	s_andn2_b32 s98, s28, 0xff
	s_add_i32 s28, s28, s99
.Lts2_setup:
	s_cmp_ge_i32 s30, s28
	s_cbranch_scc1 .LBB0_1726
	s_mov_b32 s99, s30
	s_mov_b32 s100, 0
	s_cmp_lt_i32 s30, s98
	s_cbranch_scc1 .Lts2_u1
	s_sub_i32 s99, s30, s98
	s_and_b32 s100, s99, 1
	s_add_i32 s100, s100, 1
	s_lshr_b32 s99, s99, 1
	s_add_i32 s99, s99, s98
.Lts2_u1:
	s_add_i32 s0, 0, 0x22014
	s_mov_b32 s29, -1
.LBB0_1591:
	v_mov_b32_e32 v0, s0
	ds_read_b32 v0, v0
	s_add_i32 s29, s29, 1
	s_add_i32 s0, s0, 4
	s_waitcnt lgkmcnt(0)
	v_cmp_ge_i32_e32 vcc, s99, v0
	s_cbranch_vccnz .LBB0_1591
	s_lshl_b32 s0, s29, 2
	s_add_i32 s0, s0, 0
	s_add_i32 s1, s0, 0x22094
	v_mov_b32_e32 v0, s1
	ds_read_b32 v0, v0
	s_add_i32 s1, s0, 0x22010
	v_mov_b32_e32 v1, s1
	ds_read_b32 v1, v1
	s_mov_b32 s31, 0
	s_waitcnt lgkmcnt(1)
	v_readfirstlane_b32 s1, v0
	s_abs_i32 s2, s1
	v_cvt_f32_u32_e32 v0, s2
	s_sub_i32 s6, 0, s2
	s_waitcnt lgkmcnt(0)
	v_readfirstlane_b32 s3, v1
	s_sub_i32 s3, s99, s3
	v_rcp_iflag_f32_e32 v0, v0
	s_abs_i32 s5, s3
	s_xor_b32 s4, s3, s1
	s_ashr_i32 s4, s4, 31
	v_mul_f32_e32 v0, 0x4f7ffffe, v0
	v_cvt_u32_f32_e32 v0, v0
	s_brev_b32 s10, 32
	s_movk_i32 s33, 0x80
	s_mov_b32 s34, 0x40000
	v_readfirstlane_b32 s7, v0
	s_mul_i32 s6, s6, s7
	s_mul_hi_u32 s6, s7, s6
	s_add_i32 s7, s7, s6
	s_mul_hi_u32 s6, s5, s7
	s_mul_i32 s7, s6, s2
	s_sub_i32 s5, s5, s7
	s_add_i32 s8, s6, 1
	s_sub_i32 s7, s5, s2
	s_cmp_ge_u32 s5, s2
	s_cselect_b32 s6, s8, s6
	s_cselect_b32 s5, s7, s5
	s_add_i32 s7, s6, 1
	s_cmp_ge_u32 s5, s2
	s_cselect_b32 s2, s7, s6
	s_add_i32 s0, s0, 0x22114
	v_mov_b32_e32 v0, s0
	ds_read_b32 v0, v0
	s_xor_b32 s2, s2, s4
	s_sub_i32 s26, s2, s4
	s_mul_i32 s0, s26, s1
	s_sub_i32 s0, s3, s0
	s_mov_b32 s7, 0x20000
	s_lshl_b32 s47, s0, 8
	s_waitcnt lgkmcnt(0)
	v_readfirstlane_b32 s43, v0
	s_mov_b32 s11, s7
	s_and_b32 s9, s71, 0xffff
	s_mov_b32 s8, s70
	s_mov_b64 s[2:3], 0
	s_mov_b32 s6, 0x400000
	s_mov_b32 s35, 0x60000
	s_mov_b32 s36, 0x20080
	s_mov_b32 s37, 0x40080
	s_mov_b32 s42, 0x60080
	v_mov_b32_e32 v164, 0x7d7d7d7d
	v_mov_b32_e32 v165, 0x76767676
	v_mov_b32_e32 v253, 0
	s_cmp_eq_u32 s100, 0
	s_cbranch_scc1 .Lts2_a1
	s_add_i32 s99, s47, 0x80
	s_cmp_eq_u32 s100, 1
	s_cbranch_scc0 .Lts2_b1
	s_min_i32 s43, s43, s99
	s_branch .Lts2_a1
.Lts2_b1:
	s_cmp_lt_i32 s99, s43
	s_cbranch_scc0 .Lts2_a1
	s_mov_b32 s47, s99
.Lts2_a1:
	s_mov_b32 s14, s29
	s_branch .LBB0_1594

;     ...
;     for (;;) {
;       const int un = u + nb;
;       const bool has_next = un < total;
;       int e2 = 0, m2 = 0, t2 = 0, c2 = 1;
;       if (has_next) decode(un, e2, m2, t2, c2);
;       const CfgT nxtc{p, e2, m2, t2, c2};
;       const bool tophalf = cur.cnt - cur.m0 <= 128;
;       if (pre) { if (tophalf) gemm256f8dma_unit<CfgT, true, true, PMODE>(lds, cur, has_next, nxtc); else gemm256f8dma_unit<CfgT, false, true, PMODE>(lds, cur, has_next, nxtc); }
;       else { if (tophalf) gemm256f8dma_unit<CfgT, true, false, PMODE>(lds, cur, has_next, nxtc); else gemm256f8dma_unit<CfgT, false, false, PMODE>(lds, cur, has_next, nxtc); }
;       if (!has_next) break;
;       cur.e = e2; cur.m0 = m2; cur.tn = t2; cur.cnt = c2; u = un; pre = true;
.LBB0_1594:
	s_add_i32 s30, s30, s96
	s_cmp_lt_i32 s30, s28
	s_cselect_b64 s[22:23], -1, 0
	s_cmp_ge_i32 s30, s28
	s_cselect_b64 s[0:1], -1, 0
	s_and_b64 vcc, exec, s[0:1]
	s_cbranch_vccnz .LBB0_1598
	s_mov_b32 s99, s30
	s_mov_b32 s100, 0
	s_cmp_lt_i32 s30, s98
	s_cbranch_scc1 .Lts2_u2
	s_sub_i32 s99, s30, s98
	s_and_b32 s100, s99, 1
	s_add_i32 s100, s100, 1
	s_lshr_b32 s99, s99, 1
	s_add_i32 s99, s99, s98
.Lts2_u2:
	s_lshl_b32 s4, s29, 2
	s_add_i32 s5, s29, -1
	s_add_i32 s4, s4, 0
	s_add_i32 s4, s4, 0x22014
	s_mov_b32 s29, s5
.LBB0_1596:
	v_mov_b32_e32 v0, s4
	ds_read_b32 v0, v0
	s_add_i32 s29, s29, 1
	s_add_i32 s4, s4, 4
	s_waitcnt lgkmcnt(0)
	v_cmp_ge_i32_e32 vcc, s99, v0
	s_cbranch_vccnz .LBB0_1596
	s_lshl_b32 s4, s29, 2
	s_add_i32 s4, s4, 0
	s_add_i32 s5, s4, 0x22094
	v_mov_b32_e32 v0, s5
	ds_read_b32 v0, v0
	s_add_i32 s5, s4, 0x22010
	v_mov_b32_e32 v1, s5
	ds_read_b32 v1, v1
	s_waitcnt lgkmcnt(1)
	v_readfirstlane_b32 s5, v0
	s_abs_i32 s12, s5
	v_cvt_f32_u32_e32 v0, s12
	s_sub_i32 s17, 0, s12
	s_waitcnt lgkmcnt(0)
	v_readfirstlane_b32 s13, v1
	s_sub_i32 s13, s99, s13
	v_rcp_iflag_f32_e32 v0, v0
	s_abs_i32 s16, s13
	s_xor_b32 s15, s13, s5
	s_ashr_i32 s15, s15, 31
	v_mul_f32_e32 v0, 0x4f7ffffe, v0
	v_cvt_u32_f32_e32 v0, v0
	s_nop 0
	v_readfirstlane_b32 s18, v0
	s_mul_i32 s17, s17, s18
	s_mul_hi_u32 s17, s18, s17
	s_add_i32 s18, s18, s17
	s_mul_hi_u32 s17, s16, s18
	s_mul_i32 s18, s17, s12
	s_sub_i32 s16, s16, s18
	s_add_i32 s19, s17, 1
	s_sub_i32 s18, s16, s12
	s_cmp_ge_u32 s16, s12
	s_cselect_b32 s17, s19, s17
	s_cselect_b32 s16, s18, s16
	s_add_i32 s18, s17, 1
	s_cmp_ge_u32 s16, s12
	s_cselect_b32 s12, s18, s17
	s_add_i32 s4, s4, 0x22114
	v_mov_b32_e32 v0, s4
	ds_read_b32 v0, v0
	s_xor_b32 s12, s12, s15
	s_sub_i32 s44, s12, s15
	s_mul_i32 s4, s44, s5
	s_sub_i32 s4, s13, s4
	s_lshl_b32 s46, s4, 8
	s_waitcnt lgkmcnt(0)
	v_readfirstlane_b32 s45, v0
	s_cmp_eq_u32 s100, 0
	s_cbranch_scc1 .Lts2_a2
	s_add_i32 s99, s46, 0x80
	s_cmp_eq_u32 s100, 1
	s_cbranch_scc0 .Lts2_b2
	s_min_i32 s45, s45, s99
	s_branch .Lts2_a2
.Lts2_b2:
	s_cmp_lt_i32 s99, s45
	s_cbranch_scc0 .Lts2_a2
	s_mov_b32 s46, s99
.Lts2_a2:
	s_mov_b32 s12, s29
	s_branch .LBB0_1599
